# importance-pass QK^T LDS reads software-pipelined; compressed-branch epilogue with transposed PV output (per-lane rescale, 16-byte stores); bias-partial work moved to workgroups 240-255
# baseline (speedup 1.0000x reference)
; __global__ void __launch_bounds__(NWAVES * 64, 2) hybrid_fwd(Args args) {
;     ...
;         for (int e = gt; e < DEPTH * 2 * 16 * 128; e += NGT) { const int n = e & 127, kc = (e >> 7) & 15, lk = e >> 11;
;             const float* w1 = args.in[4] + ((size_t)lk * 4096 + kc * 256) * 128 + n; const float* ps = args.in[3] + (size_t)lk * 4096 + kc * 256; float a = 0.f;
; #pragma unroll 32
;             for (int k = 0; k < 256; ++k) a += ps[k] * w1[(size_t)k * 128];
;             ((float*)(ws + WS_B1P))[e] = a; }
.LBB0_398:
	v_readlane_b32 s0, v253, 2
	s_lshl_b32 s0, s0, 9
	s_nop 0
	v_writelane_b32 v253, s0, 47
	v_add_u32_e32 v2, s0, v1
	v_add_u32_e32 v144, 0xfffe2000, v2
	s_movk_i32 s0, 0x2000
	v_cmp_gt_u32_e32 vcc, s0, v144
	s_and_saveexec_b64 s[0:1], vcc
	s_cbranch_execz .LBB0_403
	v_readlane_b32 s4, v253, 35
	v_readlane_b32 s5, v253, 36
	v_readlane_b32 s6, v253, 37
	v_readlane_b32 s7, v253, 38
	v_readlane_b32 s8, v253, 39
	v_readlane_b32 s9, v253, 40
	v_and_b32_e32 v3, 0x7f, v1
	v_readlane_b32 s16, v253, 3
	v_readlane_b32 s10, v253, 41
	v_readlane_b32 s11, v253, 42
	s_mov_b64 s[4:5], s[8:9]
	v_lshlrev_b32_e32 v4, 2, v3
	v_mov_b32_e32 v5, 0
	v_readlane_b32 s24, v253, 11
	v_readlane_b32 s25, v253, 12
	s_mov_b64 s[6:7], s[10:11]
	s_mov_b64 s[2:3], 0x3e00
	v_lshl_add_u64 v[4:5], s[24:25], 0, v[4:5]
	s_add_u32 s4, s6, 0x6b6a1000
	v_readlane_b32 s17, v253, 4
	v_readlane_b32 s18, v253, 5
	v_readlane_b32 s19, v253, 6
	v_readlane_b32 s20, v253, 7
	v_lshl_add_u64 v[4:5], v[4:5], 0, s[2:3]
	v_lshlrev_b32_e32 v1, 1, v1
	v_readlane_b32 s2, v253, 2
	s_addc_u32 s5, s7, 0
	s_addk_i32 s2, 0xff10
	s_lshl_b32 s11, s83, 10
	v_lshl_add_u32 v1, s2, 10, v1
	s_mov_b64 s[6:7], 0
	s_mov_b32 s12, 0x1e0000
	s_movk_i32 s16, 0x3c00
	s_movk_i32 s17, 0xd000
	s_movk_i32 s18, 0xe000
	s_movk_i32 s19, 0xf000
	s_mov_b64 s[8:9], 0x4000
	s_movk_i32 s20, 0x1fff
	v_mov_b32_e32 v6, v144
	v_readlane_b32 s21, v253, 8
	v_readlane_b32 s22, v253, 9
	v_readlane_b32 s23, v253, 10
	v_readlane_b32 s26, v253, 13
	v_readlane_b32 s27, v253, 14
	v_readlane_b32 s28, v253, 15
	v_readlane_b32 s29, v253, 16
	v_readlane_b32 s30, v253, 17
	v_readlane_b32 s31, v253, 18

; __device__ __forceinline__ int crow(int r, int hi) { return (r & 3) + 8 * (r >> 2) + 4 * hi; }
; __device__ __forceinline__ float at_softmax(f32x16& p0, f32x16& p1, float& m_reg, f32x16& negm, float& l_reg, bf16x8& pa0, bf16x8& pa1, bf16x8& pa2, bf16x8& pa3, bool rowsel, bool use_rowsel) {
;     ...
;     float s0 = 0.f, s1 = 0.f, s2 = 0.f, s3 = 0.f;
; #pragma unroll
;     for (int r = 0; r < 16; r += 4) { p0[r] = __builtin_amdgcn_exp2f(p0[r]); p0[r + 1] = __builtin_amdgcn_exp2f(p0[r + 1]); p0[r + 2] = __builtin_amdgcn_exp2f(p0[r + 2]); p0[r + 3] = __builtin_amdgcn_exp2f(p0[r + 3]);
;         s0 += p0[r]; s1 += p0[r + 1]; s2 += p0[r + 2]; s3 += p0[r + 3]; }
; #pragma unroll
;     for (int r = 0; r < 16; r += 4) { p1[r] = __builtin_amdgcn_exp2f(p1[r]); p1[r + 1] = __builtin_amdgcn_exp2f(p1[r + 1]); p1[r + 2] = __builtin_amdgcn_exp2f(p1[r + 2]); p1[r + 3] = __builtin_amdgcn_exp2f(p1[r + 3]);
;         s0 += p1[r]; s1 += p1[r + 1]; s2 += p1[r + 2]; s3 += p1[r + 3]; }
;     float ps = (s0 + s1) + (s2 + s3);
;     if (use_rowsel && !rowsel) ps = 0.f;
;     { auto rr = __builtin_amdgcn_permlane32_swap(__float_as_uint(ps), __float_as_uint(ps), false, false); ps = __uint_as_float(rr[0]) + __uint_as_float(rr[1]); }
;     l_reg = l_reg * alpha + ps;
;     const unsigned keep = (use_rowsel && !rowsel) ? 0u : 0xffffffffu;
;     ...
;     PK4(p0, 0, pa0); PK4(p0, 8, pa1); PK4(p1, 0, pa2); PK4(p1, 8, pa3);
; template <int MODE> ...
;     ...
;         if (__any(alpha < 1.f)) { if (hi == 0) wsl[l32] = alpha; asm volatile("s_waitcnt lgkmcnt(0)" ::: "memory");
; #pragma unroll
;             for (int d = 0; d < 4; ++d)
; #pragma unroll
;                 for (int r = 0; r < 16; ++r) o[d][r] *= wsl[crow(r, hi)]; }
.LBB0_807:
	v_exp_f32_e32 v102, v102
	v_exp_f32_e32 v103, v103
	v_exp_f32_e32 v106, v106
	v_exp_f32_e32 v107, v107
	v_exp_f32_e32 v164, v100
	v_exp_f32_e32 v165, v101
	v_exp_f32_e32 v110, v110
	v_exp_f32_e32 v111, v111
	v_exp_f32_e32 v104, v104
	v_exp_f32_e32 v105, v105
	v_exp_f32_e32 v114, v114
	v_exp_f32_e32 v115, v115
	v_add_f32_e32 v166, 0, v102
	v_add_f32_e32 v167, 0, v103
	v_exp_f32_e32 v108, v108
	v_exp_f32_e32 v109, v109
	v_exp_f32_e32 v172, v86
	v_exp_f32_e32 v173, v87
	v_add_f32_e32 v166, v106, v166
	v_add_f32_e32 v167, v107, v167
	v_exp_f32_e32 v112, v112
	v_exp_f32_e32 v113, v113
	v_add_f32_e32 v100, 0, v164
	v_add_f32_e32 v101, 0, v165
	v_add_f32_e32 v166, v110, v166
	v_add_f32_e32 v167, v111, v167
	v_exp_f32_e32 v170, v84
	v_exp_f32_e32 v171, v85
	v_add_f32_e32 v100, v104, v100
	v_add_f32_e32 v101, v105, v101
	v_add_f32_e32 v166, v114, v166
	v_add_f32_e32 v167, v115, v167
	v_exp_f32_e32 v88, v88
	v_exp_f32_e32 v89, v89
	v_exp_f32_e32 v90, v90
	v_exp_f32_e32 v91, v91
	v_add_f32_e32 v100, v108, v100
	v_add_f32_e32 v101, v109, v101
	v_add_f32_e32 v86, v172, v166
	v_add_f32_e32 v87, v173, v167
	v_exp_f32_e32 v166, v92
	v_exp_f32_e32 v167, v93
	v_exp_f32_e32 v174, v94
	v_exp_f32_e32 v175, v95
	v_add_f32_e32 v100, v112, v100
	v_add_f32_e32 v101, v113, v101
	v_exp_f32_e32 v176, v96
	v_exp_f32_e32 v177, v97
	v_exp_f32_e32 v190, v98
	v_exp_f32_e32 v191, v99
	v_add_f32_e32 v84, v170, v100
	v_add_f32_e32 v85, v171, v101
	v_add_f32_e32 v84, v88, v84
	v_add_f32_e32 v85, v89, v85
	v_add_f32_e32 v86, v90, v86
	v_add_f32_e32 v87, v91, v87
	v_add_f32_e32 v84, v166, v84
	v_add_f32_e32 v85, v167, v85
	v_add_f32_e32 v86, v174, v86
	v_add_f32_e32 v87, v175, v87
	v_add_f32_e32 v84, v176, v84
	v_add_f32_e32 v85, v177, v85
	v_add_f32_e32 v86, v190, v86
	v_add_f32_e32 v87, v191, v87
	v_add_f32_e32 v84, v85, v84
	v_add_f32_e32 v85, v87, v86
	v_add_f32_e32 v100, v85, v84
	v_mov_b32_e32 v101, v100
	v_cvt_pk_bf16_f32 v84, v164, v165
	v_cvt_pk_bf16_f32 v85, v102, v103
	v_cvt_pk_bf16_f32 v86, v104, v105
	v_cvt_pk_bf16_f32 v87, v106, v107
	v_cvt_pk_bf16_f32 v92, v108, v109
	v_cvt_pk_bf16_f32 v93, v110, v111
	v_cvt_pk_bf16_f32 v94, v112, v113
	v_cvt_pk_bf16_f32 v95, v114, v115
	v_cvt_pk_bf16_f32 v96, v170, v171
	v_cvt_pk_bf16_f32 v97, v172, v173
	v_cvt_pk_bf16_f32 v98, v88, v89
	v_cvt_pk_bf16_f32 v99, v90, v91
	v_cvt_pk_bf16_f32 v88, v166, v167
	v_cvt_pk_bf16_f32 v89, v174, v175
	v_cvt_pk_bf16_f32 v90, v176, v177
	v_cvt_pk_bf16_f32 v91, v190, v191
	s_nop 1
	v_permlane32_swap_b32_e32 v100, v101
	v_permlane32_swap_b32_e32 v84, v86
	v_permlane32_swap_b32_e32 v85, v87
	v_permlane32_swap_b32_e32 v92, v94
	v_permlane32_swap_b32_e32 v93, v95
	v_permlane32_swap_b32_e32 v96, v98
	v_permlane32_swap_b32_e32 v97, v99
	v_permlane32_swap_b32_e32 v88, v90
	v_permlane32_swap_b32_e32 v89, v91
	v_cmp_gt_f32_e32 vcc, 1.0, v2
	s_cbranch_vccz .LBB0_811
	v_pk_mul_f32 v[4:5], v[4:5], v[2:3] op_sel_hi:[1,0]
	v_pk_mul_f32 v[6:7], v[6:7], v[2:3] op_sel_hi:[1,0]
	v_pk_mul_f32 v[8:9], v[8:9], v[2:3] op_sel_hi:[1,0]
	v_pk_mul_f32 v[10:11], v[10:11], v[2:3] op_sel_hi:[1,0]
	v_pk_mul_f32 v[12:13], v[12:13], v[2:3] op_sel_hi:[1,0]
	v_pk_mul_f32 v[14:15], v[14:15], v[2:3] op_sel_hi:[1,0]
	v_pk_mul_f32 v[16:17], v[16:17], v[2:3] op_sel_hi:[1,0]
	v_pk_mul_f32 v[18:19], v[18:19], v[2:3] op_sel_hi:[1,0]
	v_pk_mul_f32 v[20:21], v[20:21], v[2:3] op_sel_hi:[1,0]
	v_pk_mul_f32 v[22:23], v[22:23], v[2:3] op_sel_hi:[1,0]
	v_pk_mul_f32 v[24:25], v[24:25], v[2:3] op_sel_hi:[1,0]
	v_pk_mul_f32 v[26:27], v[26:27], v[2:3] op_sel_hi:[1,0]
	v_pk_mul_f32 v[28:29], v[28:29], v[2:3] op_sel_hi:[1,0]
	v_pk_mul_f32 v[30:31], v[30:31], v[2:3] op_sel_hi:[1,0]
	v_pk_mul_f32 v[32:33], v[32:33], v[2:3] op_sel_hi:[1,0]
	v_pk_mul_f32 v[34:35], v[34:35], v[2:3] op_sel_hi:[1,0]
	v_pk_mul_f32 v[36:37], v[36:37], v[2:3] op_sel_hi:[1,0]
	v_pk_mul_f32 v[38:39], v[38:39], v[2:3] op_sel_hi:[1,0]
	v_pk_mul_f32 v[40:41], v[40:41], v[2:3] op_sel_hi:[1,0]
	v_pk_mul_f32 v[42:43], v[42:43], v[2:3] op_sel_hi:[1,0]
	v_pk_mul_f32 v[44:45], v[44:45], v[2:3] op_sel_hi:[1,0]
	v_pk_mul_f32 v[46:47], v[46:47], v[2:3] op_sel_hi:[1,0]
	v_pk_mul_f32 v[48:49], v[48:49], v[2:3] op_sel_hi:[1,0]
	v_pk_mul_f32 v[50:51], v[50:51], v[2:3] op_sel_hi:[1,0]
	v_pk_mul_f32 v[52:53], v[52:53], v[2:3] op_sel_hi:[1,0]
	v_pk_mul_f32 v[54:55], v[54:55], v[2:3] op_sel_hi:[1,0]
	v_pk_mul_f32 v[56:57], v[56:57], v[2:3] op_sel_hi:[1,0]
	v_pk_mul_f32 v[58:59], v[58:59], v[2:3] op_sel_hi:[1,0]
	v_pk_mul_f32 v[60:61], v[60:61], v[2:3] op_sel_hi:[1,0]
	v_pk_mul_f32 v[62:63], v[62:63], v[2:3] op_sel_hi:[1,0]
	v_pk_mul_f32 v[64:65], v[64:65], v[2:3] op_sel_hi:[1,0]
	v_pk_mul_f32 v[66:67], v[66:67], v[2:3] op_sel_hi:[1,0]
; __device__ __forceinline__ int crow(int r, int hi) { return (r & 3) + 8 * (r >> 2) + 4 * hi; }
; __device__ __forceinline__ void at_pv(f32x16 (&o)[4], int vb, bf16x8 pa0, bf16x8 pa1, bf16x8 pa2, bf16x8 pa3) {
;     ...
;     PV_D0(0); PV_D0(1); PV_D0(2); PV_D0(3);
; template <int MODE> ...
;     ...
;         const float alpha = at_softmax(p0, p1, m_reg, negm, l_reg, pa0, pa1, pa2, pa3, rowsel, MODE == 1);
;         if (__any(alpha < 1.f)) { if (hi == 0) wsl[l32] = alpha; asm volatile("s_waitcnt lgkmcnt(0)" ::: "memory");
; #pragma unroll
;             for (int d = 0; d < 4; ++d)
; #pragma unroll
;                 for (int r = 0; r < 16; ++r) o[d][r] *= wsl[crow(r, hi)]; }
;         at_pv(o, vb0 + buf * 16384, pa0, pa1, pa2, pa3);
;         }
;         stg = stg == 2 ? 0 : stg + 1;
.LBB0_811:
	v_add_f32_e32 v100, v100, v101
	v_fmac_f32_e32 v100, v189, v2
	v_add_u32_e32 v2, s30, v188
	ds_read_b64_tr_b16 v[102:103], v2 offset:0
	ds_read_b64_tr_b16 v[104:105], v2 offset:0x800
	ds_read_b64_tr_b16 v[106:107], v2 offset:0x1000
	ds_read_b64_tr_b16 v[108:109], v2 offset:0x1800
	ds_read_b64_tr_b16 v[110:111], v2 offset:0x2000
	ds_read_b64_tr_b16 v[112:113], v2 offset:0x2800
	ds_read_b64_tr_b16 v[170:171], v2 offset:0x3000
	ds_read_b64_tr_b16 v[172:173], v2 offset:0x3800
	s_waitcnt lgkmcnt(0)
	s_nop 0
	v_mfma_f32_32x32x16_bf16 v[4:19], v[102:105], v[84:87], v[4:19]
	ds_read_b64_tr_b16 v[102:103], v2 offset:0x200
	ds_read_b64_tr_b16 v[104:105], v2 offset:0xa00
	v_mfma_f32_32x32x16_bf16 v[4:19], v[106:109], v[92:95], v[4:19]
	ds_read_b64_tr_b16 v[106:107], v2 offset:0x1200
	ds_read_b64_tr_b16 v[108:109], v2 offset:0x1a00
	v_mfma_f32_32x32x16_bf16 v[4:19], v[110:113], v[96:99], v[4:19]
	ds_read_b64_tr_b16 v[110:111], v2 offset:0x2200
	ds_read_b64_tr_b16 v[112:113], v2 offset:0x2a00
	v_mfma_f32_32x32x16_bf16 v[4:19], v[170:173], v[88:91], v[4:19]
	ds_read_b64_tr_b16 v[170:171], v2 offset:0x3200
	ds_read_b64_tr_b16 v[172:173], v2 offset:0x3a00
	s_waitcnt lgkmcnt(0)
	v_mfma_f32_32x32x16_bf16 v[20:35], v[102:105], v[84:87], v[20:35]
	ds_read_b64_tr_b16 v[102:103], v2 offset:0x400
	ds_read_b64_tr_b16 v[104:105], v2 offset:0xc00
	v_mfma_f32_32x32x16_bf16 v[20:35], v[106:109], v[92:95], v[20:35]
	ds_read_b64_tr_b16 v[106:107], v2 offset:0x1400
	ds_read_b64_tr_b16 v[108:109], v2 offset:0x1c00
	v_mfma_f32_32x32x16_bf16 v[20:35], v[110:113], v[96:99], v[20:35]
	ds_read_b64_tr_b16 v[110:111], v2 offset:0x2400
	ds_read_b64_tr_b16 v[112:113], v2 offset:0x2c00
	v_mfma_f32_32x32x16_bf16 v[20:35], v[170:173], v[88:91], v[20:35]
	ds_read_b64_tr_b16 v[170:171], v2 offset:0x3400
	ds_read_b64_tr_b16 v[172:173], v2 offset:0x3c00
	s_waitcnt lgkmcnt(0)
	v_mfma_f32_32x32x16_bf16 v[36:51], v[102:105], v[84:87], v[36:51]
	ds_read_b64_tr_b16 v[102:103], v2 offset:0x600
	ds_read_b64_tr_b16 v[104:105], v2 offset:0xe00
	v_mfma_f32_32x32x16_bf16 v[36:51], v[106:109], v[92:95], v[36:51]
	ds_read_b64_tr_b16 v[106:107], v2 offset:0x1600
	ds_read_b64_tr_b16 v[108:109], v2 offset:0x1e00
	v_mfma_f32_32x32x16_bf16 v[36:51], v[110:113], v[96:99], v[36:51]
	ds_read_b64_tr_b16 v[110:111], v2 offset:0x2600
	ds_read_b64_tr_b16 v[112:113], v2 offset:0x2e00
	v_mfma_f32_32x32x16_bf16 v[36:51], v[170:173], v[88:91], v[36:51]
	ds_read_b64_tr_b16 v[170:171], v2 offset:0x3600
	ds_read_b64_tr_b16 v[172:173], v2 offset:0x3e00
	s_waitcnt lgkmcnt(0)
	v_mfma_f32_32x32x16_bf16 v[52:67], v[102:105], v[84:87], v[52:67]
	s_add_i32 s10, s19, 1
	s_cmp_lg_u32 s19, 2
	s_cselect_b32 s19, s10, 0
	s_add_i32 s20, s20, 64
	s_add_u32 s8, s8, 0x4000
	s_addc_u32 s9, s9, 0
	s_add_i32 s10, s21, 1
	v_mfma_f32_32x32x16_bf16 v[52:67], v[106:109], v[92:95], v[52:67]
	s_cmp_eq_u32 s21, s16
	v_mfma_f32_32x32x16_bf16 v[52:67], v[110:113], v[96:99], v[52:67]
	v_mfma_f32_32x32x16_bf16 v[52:67], v[170:173], v[88:91], v[52:67]
	s_cbranch_scc1 .LBB0_814
	s_mov_b32 s21, s10
	v_mov_b32_e32 v189, v100
	s_cmp_ge_i32 s21, s16
	s_mov_b64 s[10:11], -1
	s_cbranch_scc1 .LBB0_795
	s_branch .LBB0_796

; __device__ __forceinline__ unsigned f2bf(float f) { unsigned u = __builtin_bit_cast(unsigned, f); return (u + 0x7fffu + ((u >> 16) & 1u)) >> 16; }
; __device__ __forceinline__ int crow(int r, int hi) { return (r & 3) + 8 * (r >> 2) + 4 * hi; }
; template <int MODE> ...
;     ...
;     asm volatile("s_waitcnt lgkmcnt(0)" ::: "memory");
;     if (hi == 0) wsl[32 + l32] = l_reg > 0.f ? 1.f / l_reg : 0.f;
;     asm volatile("s_waitcnt lgkmcnt(0)" ::: "memory");
; #pragma unroll
;     for (int r = 0; r < 16; ++r) { const int q = crow(r, hi); const float rli = wsl[32 + q]; bf16* op = Obase + (size_t)(8 * wave + (q >> 2)) * 2048 + (q & 3) * 128 + l32;
; #pragma unroll
;         for (int d0 = 0; d0 < 4; ++d0) op[d0 * 32] = (bf16)f2bf(o[d0][r] * rli); }
;     m_out = m_reg; l_out = l_reg;
.LBB0_814:
	s_waitcnt lgkmcnt(0)
	s_xor_b64 s[96:97], s[6:7], -1
	s_ashr_i32 s93, s92, 31
	s_lshl_b64 s[2:3], s[92:93], 12
	s_add_u32 s90, s25, s2
	s_addc_u32 s91, s26, s3
	v_div_scale_f32 v2, s[6:7], v100, v100, 1.0
	v_rcp_f32_e32 v68, v2
	v_div_scale_f32 v69, vcc, 1.0, v100, 1.0
	v_fma_f32 v71, -v2, v68, 1.0
	v_fmac_f32_e32 v68, v71, v68
	v_mul_f32_e32 v71, v69, v68
	v_fma_f32 v233, -v2, v71, v69
	v_fmac_f32_e32 v71, v233, v68
	v_fma_f32 v2, -v2, v71, v69
	v_div_fmas_f32 v2, v2, v68, v71
	v_div_fixup_f32 v70, v2, v100, 1.0
	v_cmp_lt_f32_e32 vcc, 0, v100
	s_nop 1
	v_cndmask_b32_e32 v2, 0, v70, vcc
	s_mov_b32 s2, 0x07060302
	v_lshrrev_b32_e32 v232, 2, v123
	v_lshl_or_b32 v232, s14, 3, v232
	v_lshlrev_b32_e32 v232, 12, v232
	v_and_b32_e32 v68, 3, v123
	v_lshl_or_b32 v232, v68, 8, v232
	v_lshl_or_b32 v232, v124, 4, v232
	v_mul_f32_e32 v210, v4, v2
	v_mul_f32_e32 v211, v5, v2
	v_mul_f32_e32 v212, v6, v2
	v_mul_f32_e32 v213, v7, v2
	v_bfe_u32 v214, v210, 16, 1
	v_bfe_u32 v215, v211, 16, 1
	v_bfe_u32 v216, v212, 16, 1
	v_bfe_u32 v217, v213, 16, 1
	v_add3_u32 v210, v210, v214, s72
	v_add3_u32 v211, v211, v215, s72
	v_add3_u32 v212, v212, v216, s72
	v_add3_u32 v213, v213, v217, s72
	v_perm_b32 v202, v211, v210, s2
	v_perm_b32 v203, v213, v212, s2
	v_mul_f32_e32 v210, v8, v2
	v_mul_f32_e32 v211, v9, v2
	v_mul_f32_e32 v212, v10, v2
	v_mul_f32_e32 v213, v11, v2
	v_bfe_u32 v214, v210, 16, 1
	v_bfe_u32 v215, v211, 16, 1
	v_bfe_u32 v216, v212, 16, 1
	v_bfe_u32 v217, v213, 16, 1
	v_add3_u32 v210, v210, v214, s72
	v_add3_u32 v211, v211, v215, s72
	v_add3_u32 v212, v212, v216, s72
	v_add3_u32 v213, v213, v217, s72
	v_perm_b32 v204, v211, v210, s2
	v_perm_b32 v205, v213, v212, s2
	v_mul_f32_e32 v210, v12, v2
	v_mul_f32_e32 v211, v13, v2
	v_mul_f32_e32 v212, v14, v2
	v_mul_f32_e32 v213, v15, v2
	v_bfe_u32 v214, v210, 16, 1
	v_bfe_u32 v215, v211, 16, 1
	v_bfe_u32 v216, v212, 16, 1
	v_bfe_u32 v217, v213, 16, 1
	v_add3_u32 v210, v210, v214, s72
	v_add3_u32 v211, v211, v215, s72
	v_add3_u32 v212, v212, v216, s72
	v_add3_u32 v213, v213, v217, s72
	v_perm_b32 v206, v211, v210, s2
	v_perm_b32 v207, v213, v212, s2
	v_mul_f32_e32 v210, v16, v2
	v_mul_f32_e32 v211, v17, v2
	v_mul_f32_e32 v212, v18, v2
	v_mul_f32_e32 v213, v19, v2
	v_bfe_u32 v214, v210, 16, 1
	v_bfe_u32 v215, v211, 16, 1
	v_bfe_u32 v216, v212, 16, 1
	v_bfe_u32 v217, v213, 16, 1
	v_add3_u32 v210, v210, v214, s72
	v_add3_u32 v211, v211, v215, s72
	v_add3_u32 v212, v212, v216, s72
	v_add3_u32 v213, v213, v217, s72
	v_perm_b32 v208, v211, v210, s2
	v_perm_b32 v209, v213, v212, s2
	s_nop 1
	v_permlane32_swap_b32_e32 v202, v204
	v_permlane32_swap_b32_e32 v203, v205
	v_permlane32_swap_b32_e32 v206, v208
	v_permlane32_swap_b32_e32 v207, v209
	global_store_dwordx4 v232, v[202:205], s[90:91] offset:0
	global_store_dwordx4 v232, v[206:209], s[90:91] offset:32
	s_nop 1
	v_mul_f32_e32 v210, v20, v2
	v_mul_f32_e32 v211, v21, v2
	v_mul_f32_e32 v212, v22, v2
	v_mul_f32_e32 v213, v23, v2
	v_bfe_u32 v214, v210, 16, 1
	v_bfe_u32 v215, v211, 16, 1
	v_bfe_u32 v216, v212, 16, 1
	v_bfe_u32 v217, v213, 16, 1
	v_add3_u32 v210, v210, v214, s72
	v_add3_u32 v211, v211, v215, s72
	v_add3_u32 v212, v212, v216, s72
	v_add3_u32 v213, v213, v217, s72
	v_perm_b32 v202, v211, v210, s2
	v_perm_b32 v203, v213, v212, s2
	v_mul_f32_e32 v210, v24, v2
	v_mul_f32_e32 v211, v25, v2
	v_mul_f32_e32 v212, v26, v2
	v_mul_f32_e32 v213, v27, v2
	v_bfe_u32 v214, v210, 16, 1
	v_bfe_u32 v215, v211, 16, 1
	v_bfe_u32 v216, v212, 16, 1
	v_bfe_u32 v217, v213, 16, 1
	v_add3_u32 v210, v210, v214, s72
	v_add3_u32 v211, v211, v215, s72
	v_add3_u32 v212, v212, v216, s72
	v_add3_u32 v213, v213, v217, s72
	v_perm_b32 v204, v211, v210, s2
	v_perm_b32 v205, v213, v212, s2
	v_mul_f32_e32 v210, v28, v2
	v_mul_f32_e32 v211, v29, v2
	v_mul_f32_e32 v212, v30, v2
	v_mul_f32_e32 v213, v31, v2
	v_bfe_u32 v214, v210, 16, 1
	v_bfe_u32 v215, v211, 16, 1
	v_bfe_u32 v216, v212, 16, 1
	v_bfe_u32 v217, v213, 16, 1
	v_add3_u32 v210, v210, v214, s72
	v_add3_u32 v211, v211, v215, s72
	v_add3_u32 v212, v212, v216, s72
	v_add3_u32 v213, v213, v217, s72
	v_perm_b32 v206, v211, v210, s2
	v_perm_b32 v207, v213, v212, s2
	v_mul_f32_e32 v210, v32, v2
	v_mul_f32_e32 v211, v33, v2
	v_mul_f32_e32 v212, v34, v2
	v_mul_f32_e32 v213, v35, v2
	v_bfe_u32 v214, v210, 16, 1
	v_bfe_u32 v215, v211, 16, 1
	v_bfe_u32 v216, v212, 16, 1
	v_bfe_u32 v217, v213, 16, 1
	v_add3_u32 v210, v210, v214, s72
	v_add3_u32 v211, v211, v215, s72
	v_add3_u32 v212, v212, v216, s72
	v_add3_u32 v213, v213, v217, s72
	v_perm_b32 v208, v211, v210, s2
	v_perm_b32 v209, v213, v212, s2
	s_nop 1
	v_permlane32_swap_b32_e32 v202, v204
	v_permlane32_swap_b32_e32 v203, v205
	v_permlane32_swap_b32_e32 v206, v208
	v_permlane32_swap_b32_e32 v207, v209
	global_store_dwordx4 v232, v[202:205], s[90:91] offset:64
	global_store_dwordx4 v232, v[206:209], s[90:91] offset:96
	s_nop 1
	v_mul_f32_e32 v210, v36, v2
	v_mul_f32_e32 v211, v37, v2
	v_mul_f32_e32 v212, v38, v2
	v_mul_f32_e32 v213, v39, v2
	v_bfe_u32 v214, v210, 16, 1
	v_bfe_u32 v215, v211, 16, 1
	v_bfe_u32 v216, v212, 16, 1
	v_bfe_u32 v217, v213, 16, 1
	v_add3_u32 v210, v210, v214, s72
	v_add3_u32 v211, v211, v215, s72
	v_add3_u32 v212, v212, v216, s72
	v_add3_u32 v213, v213, v217, s72
	v_perm_b32 v202, v211, v210, s2
	v_perm_b32 v203, v213, v212, s2
	v_mul_f32_e32 v210, v40, v2
	v_mul_f32_e32 v211, v41, v2
	v_mul_f32_e32 v212, v42, v2
	v_mul_f32_e32 v213, v43, v2
	v_bfe_u32 v214, v210, 16, 1
	v_bfe_u32 v215, v211, 16, 1
	v_bfe_u32 v216, v212, 16, 1
	v_bfe_u32 v217, v213, 16, 1
	v_add3_u32 v210, v210, v214, s72
	v_add3_u32 v211, v211, v215, s72
	v_add3_u32 v212, v212, v216, s72
; #define GAS __attribute__((address_space(1)))
; #define LAS __attribute__((address_space(3)))
; __device__ __forceinline__ unsigned f2bf(float f) { unsigned u = __builtin_bit_cast(unsigned, f); return (u + 0x7fffu + ((u >> 16) & 1u)) >> 16; }
; __device__ __forceinline__ int crow(int r, int hi) { return (r & 3) + 8 * (r >> 2) + 4 * hi; }
; template <int MODE> ...
;     ...
;     asm volatile("s_waitcnt lgkmcnt(0)" ::: "memory");
;     if (hi == 0) wsl[32 + l32] = l_reg > 0.f ? 1.f / l_reg : 0.f;
;     asm volatile("s_waitcnt lgkmcnt(0)" ::: "memory");
; #pragma unroll
;     for (int r = 0; r < 16; ++r) { const int q = crow(r, hi); const float rli = wsl[32 + q]; bf16* op = Obase + (size_t)(8 * wave + (q >> 2)) * 2048 + (q & 3) * 128 + l32;
; #pragma unroll
;         for (int d0 = 0; d0 < 4; ++d0) op[d0 * 32] = (bf16)f2bf(o[d0][r] * rli); }
;     m_out = m_reg; l_out = l_reg;
; __device__ __forceinline__ void at_importance(LAS unsigned char* lds, const bf16x8 (&qr)[8], const bf16* Kb, int nct, int lim, float m_reg, float l_reg, int tid_in) {
;     ...
;     const int sr = tid >> 4, sc = (tid & 15) * 8, kws = KSWZ(sr, sc * 2);
;     const int head = l32 & 3, tok = 8 * wave + (l32 >> 2);
;     const float linv = l_reg > 0.f ? 1.f / l_reg : 0.f; const f32x16 zero16 = {};
;     bf16x8 st_k0, st_k1;
;     __syncthreads();
;     if (tid < 256) carry[tid] = 0.f;
;     { const bf16* kp_ = Kb + (size_t)sr * 128 + sc; st_k0 = *(const GAS bf16x8*)kp_; st_k1 = *(const GAS bf16x8*)(kp_ + 32 * 128); }
;     *(LAS bf16x8*)(K_lds + kws) = st_k0; *(LAS bf16x8*)(K_lds + kws + 32 * 256) = st_k1;
;     __syncthreads();
	v_add3_u32 v213, v213, v217, s72
	v_perm_b32 v204, v211, v210, s2
	v_perm_b32 v205, v213, v212, s2
	v_mul_f32_e32 v210, v44, v2
	v_mul_f32_e32 v211, v45, v2
	v_mul_f32_e32 v212, v46, v2
	v_mul_f32_e32 v213, v47, v2
	v_bfe_u32 v214, v210, 16, 1
	v_bfe_u32 v215, v211, 16, 1
	v_bfe_u32 v216, v212, 16, 1
	v_bfe_u32 v217, v213, 16, 1
	v_add3_u32 v210, v210, v214, s72
	v_add3_u32 v211, v211, v215, s72
	v_add3_u32 v212, v212, v216, s72
	v_add3_u32 v213, v213, v217, s72
	v_perm_b32 v206, v211, v210, s2
	v_perm_b32 v207, v213, v212, s2
	v_mul_f32_e32 v210, v48, v2
	v_mul_f32_e32 v211, v49, v2
	v_mul_f32_e32 v212, v50, v2
	v_mul_f32_e32 v213, v51, v2
	v_bfe_u32 v214, v210, 16, 1
	v_bfe_u32 v215, v211, 16, 1
	v_bfe_u32 v216, v212, 16, 1
	v_bfe_u32 v217, v213, 16, 1
	v_add3_u32 v210, v210, v214, s72
	v_add3_u32 v211, v211, v215, s72
	v_add3_u32 v212, v212, v216, s72
	v_add3_u32 v213, v213, v217, s72
	v_perm_b32 v208, v211, v210, s2
	v_perm_b32 v209, v213, v212, s2
	s_nop 1
	v_permlane32_swap_b32_e32 v202, v204
	v_permlane32_swap_b32_e32 v203, v205
	v_permlane32_swap_b32_e32 v206, v208
	v_permlane32_swap_b32_e32 v207, v209
	global_store_dwordx4 v232, v[202:205], s[90:91] offset:128
	global_store_dwordx4 v232, v[206:209], s[90:91] offset:160
	s_nop 1
	v_mul_f32_e32 v210, v52, v2
	v_mul_f32_e32 v211, v53, v2
	v_mul_f32_e32 v212, v54, v2
	v_mul_f32_e32 v213, v55, v2
	v_bfe_u32 v214, v210, 16, 1
	v_bfe_u32 v215, v211, 16, 1
	v_bfe_u32 v216, v212, 16, 1
	v_bfe_u32 v217, v213, 16, 1
	v_add3_u32 v210, v210, v214, s72
	v_add3_u32 v211, v211, v215, s72
	v_add3_u32 v212, v212, v216, s72
	v_add3_u32 v213, v213, v217, s72
	v_perm_b32 v202, v211, v210, s2
	v_perm_b32 v203, v213, v212, s2
	v_mul_f32_e32 v210, v56, v2
	v_mul_f32_e32 v211, v57, v2
	v_mul_f32_e32 v212, v58, v2
	v_mul_f32_e32 v213, v59, v2
	v_bfe_u32 v214, v210, 16, 1
	v_bfe_u32 v215, v211, 16, 1
	v_bfe_u32 v216, v212, 16, 1
	v_bfe_u32 v217, v213, 16, 1
	v_add3_u32 v210, v210, v214, s72
	v_add3_u32 v211, v211, v215, s72
	v_add3_u32 v212, v212, v216, s72
	v_add3_u32 v213, v213, v217, s72
	v_perm_b32 v204, v211, v210, s2
	v_perm_b32 v205, v213, v212, s2
	v_mul_f32_e32 v210, v60, v2
	v_mul_f32_e32 v211, v61, v2
	v_mul_f32_e32 v212, v62, v2
	v_mul_f32_e32 v213, v63, v2
	v_bfe_u32 v214, v210, 16, 1
	v_bfe_u32 v215, v211, 16, 1
	v_bfe_u32 v216, v212, 16, 1
	v_bfe_u32 v217, v213, 16, 1
	v_add3_u32 v210, v210, v214, s72
	v_add3_u32 v211, v211, v215, s72
	v_add3_u32 v212, v212, v216, s72
	v_add3_u32 v213, v213, v217, s72
	v_perm_b32 v206, v211, v210, s2
	v_perm_b32 v207, v213, v212, s2
	v_mul_f32_e32 v210, v64, v2
	v_mul_f32_e32 v211, v65, v2
	v_mul_f32_e32 v212, v66, v2
	v_mul_f32_e32 v213, v67, v2
	v_bfe_u32 v214, v210, 16, 1
	v_bfe_u32 v215, v211, 16, 1
	v_bfe_u32 v216, v212, 16, 1
	v_bfe_u32 v217, v213, 16, 1
	v_add3_u32 v210, v210, v214, s72
	v_add3_u32 v211, v211, v215, s72
	v_add3_u32 v212, v212, v216, s72
	v_add3_u32 v213, v213, v217, s72
	v_perm_b32 v208, v211, v210, s2
	v_perm_b32 v209, v213, v212, s2
	s_nop 1
	v_permlane32_swap_b32_e32 v202, v204
	v_permlane32_swap_b32_e32 v203, v205
	v_permlane32_swap_b32_e32 v206, v208
	v_permlane32_swap_b32_e32 v207, v209
	global_store_dwordx4 v232, v[202:205], s[90:91] offset:192
	global_store_dwordx4 v232, v[206:209], s[90:91] offset:224
	s_nop 1
	v_mov_b32_e32 v4, v169
	s_movk_i32 s2, 0x100
	s_waitcnt vmcnt(0)
	v_readfirstlane_b32 s8, v4
	v_cmp_gt_i32_e64 s[2:3], s2, v4
	s_barrier
	s_and_saveexec_b64 s[6:7], s[2:3]
	v_lshl_add_u32 v2, v4, 2, 0
	v_add_u32_e32 v2, 0x20900, v2
	ds_write_b32 v2, v3
	s_or_b64 exec, exec, s[6:7]
	v_ashrrev_i32_e32 v44, 4, v4
	v_lshlrev_b32_e32 v2, 3, v4
	v_ashrrev_i32_e32 v45, 31, v44
	v_and_b32_e32 v2, 0x78, v2
	v_lshlrev_b64 v[6:7], 8, v[44:45]
	v_lshlrev_b32_e32 v2, 1, v2
	v_lshl_add_u64 v[6:7], s[62:63], 0, v[6:7]
	v_lshl_add_u64 v[6:7], v[6:7], 0, v[2:3]
	v_add_co_u32_e32 v8, vcc, 0x2000, v6
	s_movk_i32 s6, 0x70
	s_nop 0
	v_addc_co_u32_e32 v9, vcc, 0, v7, vcc
	global_load_dwordx4 v[36:39], v[6:7], off
	global_load_dwordx4 v[40:43], v[8:9], off
	v_lshlrev_b32_e32 v5, 8, v44
	v_bitop3_b32 v6, v2, v4, s6 bitop3:0x78
	v_add3_u32 v45, 0, v6, v5
	s_andn2_b64 vcc, exec, s[0:1]
	s_waitcnt vmcnt(1)
	ds_write_b128 v45, v[36:39]
	s_waitcnt vmcnt(0)
	ds_write_b128 v45, v[40:43] offset:8192
	s_waitcnt lgkmcnt(0)
	s_barrier
	s_cbranch_vccnz .LBB0_829
	v_bfe_u32 v7, v4, 5, 1
	v_lshlrev_b32_e32 v49, 2, v7
	v_lshlrev_b32_e32 v7, 4, v7
	v_lshlrev_b32_e32 v9, 4, v4
	s_movk_i32 s1, 0x70
	v_lshlrev_b32_e32 v5, 2, v4
	s_add_i32 s0, 0, 0x20900
	v_and_b32_e32 v10, 0x70, v9
	v_bitop3_b32 v51, v7, v9, s1 bitop3:0x78
	s_movk_i32 s1, 0x60
	v_lshl_add_u64 v[46:47], s[62:63], 0, v[2:3]
	v_add_u32_e32 v2, s0, v5
	v_and_b32_e32 v6, 31, v4
	s_lshr_b32 s0, s8, 3
	v_bfe_u32 v8, v4, 2, 3
	v_bitop3_b32 v54, v7, v10, s1 bitop3:0x36
	v_lshlrev_b32_e32 v55, 6, v4
	s_movk_i32 s1, 0xc0
	s_and_b32 s0, s0, 0x3fffff8
	v_lshl_add_u32 v50, v6, 8, 0
	v_and_or_b32 v6, v55, s1, v8
	s_add_i32 s17, 0, 0x10000
	v_add_lshl_u32 v6, v6, s0, 6
	v_add3_u32 v56, 0, v49, v6
	v_add3_u32 v57, s17, v49, v6
	v_and_b32_e32 v6, 15, v4
	v_add_u32_e32 v4, 0x200, v4
	s_mov_b32 s0, 0x3ffffff0
	v_bitop3_b32 v52, v7, v10, 32 bitop3:0x36
	v_bitop3_b32 v53, v7, v10, 64 bitop3:0x36
	v_ashrrev_i32_e32 v63, 4, v4
	v_lshlrev_b32_e32 v7, 2, v4
	v_and_or_b32 v4, v4, s0, v6
	v_lshlrev_b32_e32 v4, 2, v4
	v_add_u32_e32 v58, 0, v5
	v_add_u32_e32 v5, s17, v5
	s_movk_i32 s1, 0x204
	v_add_u32_e32 v65, 0, v4
	v_add_u32_e32 v4, s17, v4
	v_cmp_lt_f32_e32 vcc, 0, v100
	v_cmp_eq_u32_e64 s[6:7], 0, v6
	v_add_u32_e32 v59, -4, v5
	v_add_u32_e32 v60, 0xffc, v5
	v_add_u32_e32 v61, 0x1ffc, v5
	v_add_u32_e32 v62, 0x2ffc, v5
	v_mul_lo_u32 v5, v44, s1
	v_add_u32_e32 v66, 0xffc, v4
	v_add_u32_e32 v67, 0x1ffc, v4
	v_add_u32_e32 v68, 0x2ffc, v4
	v_mul_lo_u32 v4, v63, s1
	v_lshlrev_b32_e32 v6, 2, v6
	v_readlane_b32 s0, v254, 58
	v_cndmask_b32_e32 v48, 0, v70, vcc
	s_mov_b32 s18, 0
	v_add3_u32 v64, s17, v7, -4
	s_add_i32 s19, s16, 1
	v_add3_u32 v69, v4, v6, s0
	v_add3_u32 v70, v5, v6, s0
	v_add_u32_e32 v71, 64, v44
	s_movk_i32 s20, 0x100
	s_mov_b32 s21, 0
	s_branch .LBB0_823

; #define GAS __attribute__((address_space(1)))
; #define LAS __attribute__((address_space(3)))
; __device__ __forceinline__ void at_qkt(f32x16& p0, f32x16& p1, const LAS unsigned char* Kt, int l32, int hi, const bf16x8 (&qr)[8], const f32x16& cinit) {
;     const LAS unsigned char* kb[4];
; #pragma unroll
;     for (int dd = 0; dd < 4; ++dd) kb[dd] = Kt + KSWZ(l32, (dd * 16 + hi * 8) * 2);
; #pragma unroll
;     for (int d0 = 0; d0 < 8; ++d0) { const LAS unsigned char* a = kb[d0 & 3] + (d0 >> 2) * 128;
;         const bf16x8 b0 = *(const LAS bf16x8*)a, b1 = *(const LAS bf16x8*)(a + 32 * 256);
;         if (d0 == 0) { p0 = __builtin_amdgcn_mfma_f32_32x32x16_bf16(b0, qr[0], cinit, 0, 0, 0); p1 = __builtin_amdgcn_mfma_f32_32x32x16_bf16(b1, qr[0], cinit, 0, 0, 0); }
;         else { p0 = __builtin_amdgcn_mfma_f32_32x32x16_bf16(b0, qr[d0], p0, 0, 0, 0); p1 = __builtin_amdgcn_mfma_f32_32x32x16_bf16(b1, qr[d0], p1, 0, 0, 0); } }
; __device__ __forceinline__ void at_importance(LAS unsigned char* lds, const bf16x8 (&qr)[8], const bf16* Kb, int nct, int lim, float m_reg, float l_reg, int tid_in) {
;     ...
;     for (int t = 0; t < nct; ++t) {
;         const int buf = t & 1;
;         if (t + 1 < nct) { const bf16* kp_ = Kb + (size_t)(64 * (t + 1) + sr) * 128 + sc; st_k0 = *(const GAS bf16x8*)kp_; st_k1 = *(const GAS bf16x8*)(kp_ + 32 * 128); }
;         f32x16 p0, p1;
;         at_qkt(p0, p1, K_lds + buf * 16384, l32, hi, qr, zero16);
;         at_mask<0>(p0, p1, 64 * t, hi, 0, lim, true);
.LBB0_825:
	s_and_b32 s30, s21, 1
	s_lshl_b32 s31, s30, 14
	v_add_u32_e32 v76, s31, v50
	v_add_u32_e32 v77, v76, v51
	v_add_u32_e32 v78, v76, v52
	v_add_u32_e32 v79, v76, v53
	v_add_u32_e32 v76, v76, v54
	ds_read_b128 v[72:75], v77
	ds_read_b128 v[202:205], v77 offset:8192
	ds_read_b128 v[206:209], v78
	ds_read_b128 v[210:213], v78 offset:8192
	ds_read_b128 v[232:235], v79
	ds_read_b128 v[236:239], v79 offset:8192
	ds_read_b128 v[240:243], v76
	ds_read_b128 v[244:247], v76 offset:8192
	s_waitcnt lgkmcnt(7)
	v_mfma_f32_32x32x16_bf16 v[4:19], v[72:75], v[130:133], 0
	ds_read_b128 v[72:75], v77 offset:128
	s_waitcnt lgkmcnt(7)
	v_mfma_f32_32x32x16_bf16 v[20:35], v[202:205], v[130:133], 0
	ds_read_b128 v[202:205], v77 offset:8320
	s_waitcnt lgkmcnt(7)
	v_mfma_f32_32x32x16_bf16 v[4:19], v[206:209], v[134:137], v[4:19]
	ds_read_b128 v[206:209], v78 offset:128
	s_waitcnt lgkmcnt(7)
	v_mfma_f32_32x32x16_bf16 v[20:35], v[210:213], v[134:137], v[20:35]
	ds_read_b128 v[210:213], v78 offset:8320
	s_waitcnt lgkmcnt(7)
	v_mfma_f32_32x32x16_bf16 v[4:19], v[232:235], v[138:141], v[4:19]
	ds_read_b128 v[232:235], v79 offset:128
	s_waitcnt lgkmcnt(7)
	v_mfma_f32_32x32x16_bf16 v[20:35], v[236:239], v[138:141], v[20:35]
	ds_read_b128 v[236:239], v79 offset:8320
	s_waitcnt lgkmcnt(7)
	v_mfma_f32_32x32x16_bf16 v[4:19], v[240:243], v[142:145], v[4:19]
	ds_read_b128 v[240:243], v76 offset:128
	s_waitcnt lgkmcnt(7)
	v_mfma_f32_32x32x16_bf16 v[20:35], v[244:247], v[142:145], v[20:35]
	ds_read_b128 v[244:247], v76 offset:8320
	s_waitcnt lgkmcnt(7)
	v_mfma_f32_32x32x16_bf16 v[4:19], v[72:75], v[146:149], v[4:19]
	s_waitcnt lgkmcnt(6)
	v_mfma_f32_32x32x16_bf16 v[20:35], v[202:205], v[146:149], v[20:35]
	s_waitcnt lgkmcnt(5)
	v_mfma_f32_32x32x16_bf16 v[4:19], v[206:209], v[150:153], v[4:19]
	s_waitcnt lgkmcnt(4)
	v_mfma_f32_32x32x16_bf16 v[20:35], v[210:213], v[150:153], v[20:35]
	s_waitcnt lgkmcnt(3)
	v_mfma_f32_32x32x16_bf16 v[4:19], v[232:235], v[154:157], v[4:19]
	s_waitcnt lgkmcnt(2)
	v_mfma_f32_32x32x16_bf16 v[20:35], v[236:239], v[154:157], v[20:35]
	s_waitcnt lgkmcnt(1)
	v_mfma_f32_32x32x16_bf16 v[4:19], v[240:243], v[158:161], v[4:19]
	v_add_u32_e32 v72, s18, v49
	v_cmp_le_i32_e32 vcc, v72, v1
	v_add_u32_e32 v73, 2, v72
	v_cmp_lt_i32_e64 s[10:11], v72, v1
	v_cmp_lt_i32_e64 s[14:15], v72, v121
	v_cmp_le_i32_e64 s[8:9], v72, v121
	s_nop 5
	v_cndmask_b32_e32 v4, v226, v4, vcc
	s_waitcnt lgkmcnt(0)
; #define LAS __attribute__((address_space(3)))
; template <int MODE>
; __device__ __forceinline__ void at_mask(f32x16& p0, f32x16& p1, int kb, int hi, int tq, int lim, bool rowsel) {
;     const float NEG = -__builtin_inff();
; #pragma unroll
;     for (int r = 0; r < 16; ++r) { const int k0 = kb + (r & 3) + 8 * (r >> 2) + 4 * hi, k1 = k0 + 32;
;         bool v0, v1;
;         if (MODE == 0) { v0 = k0 <= lim; v1 = k1 <= lim; }
;         else if (MODE == 1) { v0 = rowsel && k0 <= tq; v1 = rowsel && k1 <= tq; }
;         else { v0 = (unsigned)(tq - k0) < (unsigned)WIN; v1 = (unsigned)(tq - k1) < (unsigned)WIN; }
;         if (!v0) p0[r] = NEG; if (!v1) p1[r] = NEG; }
; }
; __device__ __forceinline__ void at_importance(LAS unsigned char* lds, const bf16x8 (&qr)[8], const bf16* Kb, int nct, int lim, float m_reg, float l_reg, int tid_in) {
;     ...
;         at_mask<0>(p0, p1, 64 * t, hi, 0, lim, true);
; #pragma unroll
;         for (int r = 0; r < 16; ++r) { p0[r] = __builtin_amdgcn_exp2f(p0[r] - m_reg) * linv; p1[r] = __builtin_amdgcn_exp2f(p1[r] - m_reg) * linv; }
;         LAS float* sp = S4L + (head * 64 + tok) * 16 + hi; LAS float* lp = LASTL + (head * 64 + tok) * 16 + hi;
; #pragma unroll
;         for (int q = 0; q < 4; ++q) { sp[2 * q] = (p0[4 * q] + p0[4 * q + 1]) + (p0[4 * q + 2] + p0[4 * q + 3]); lp[2 * q] = p0[4 * q + 3];
;                                       sp[8 + 2 * q] = (p1[4 * q] + p1[4 * q + 1]) + (p1[4 * q + 2] + p1[4 * q + 3]); lp[8 + 2 * q] = p1[4 * q + 3]; }
;         if (t + 1 < nct) { *(LAS bf16x8*)(K_lds + (buf ^ 1) * 16384 + kws) = st_k0; *(LAS bf16x8*)(K_lds + (buf ^ 1) * 16384 + kws + 32 * 256) = st_k1; }
	v_mfma_f32_32x32x16_bf16 v[20:35], v[244:247], v[158:161], v[20:35]
	v_cmp_le_i32_e32 vcc, v73, v1
	v_cndmask_b32_e64 v5, v226, v5, s[10:11]
	v_sub_f32_e32 v5, v5, v122
	v_cndmask_b32_e32 v6, v226, v6, vcc
	v_cmp_le_i32_e32 vcc, v73, v121
	v_add_u32_e32 v73, 3, v72
	v_sub_f32_e32 v4, v4, v122
	s_nop 4
	v_cndmask_b32_e32 v22, v226, v22, vcc
	v_cmp_le_i32_e32 vcc, v73, v1
	v_cndmask_b32_e64 v21, v226, v21, s[14:15]
	v_exp_f32_e32 v5, v5
	v_cndmask_b32_e32 v7, v226, v7, vcc
	v_cmp_le_i32_e32 vcc, v73, v121
	v_add_u32_e32 v73, 8, v72
	v_sub_f32_e32 v7, v7, v122
	v_cndmask_b32_e32 v23, v226, v23, vcc
	v_cmp_le_i32_e32 vcc, v73, v1
	v_sub_f32_e32 v6, v6, v122
	v_exp_f32_e32 v7, v7
	v_cndmask_b32_e32 v8, v226, v8, vcc
	v_cmp_le_i32_e32 vcc, v73, v121
	v_add_u32_e32 v73, 9, v72
	v_sub_f32_e32 v8, v8, v122
	v_cndmask_b32_e32 v24, v226, v24, vcc
	v_cmp_le_i32_e32 vcc, v73, v1
	v_cndmask_b32_e64 v20, v226, v20, s[8:9]
	v_exp_f32_e32 v4, v4
	v_cndmask_b32_e32 v9, v226, v9, vcc
	v_cmp_le_i32_e32 vcc, v73, v121
	v_add_u32_e32 v73, 10, v72
	v_sub_f32_e32 v9, v9, v122
	v_cndmask_b32_e32 v25, v226, v25, vcc
	v_cmp_le_i32_e32 vcc, v73, v1
	v_exp_f32_e32 v9, v9
	v_sub_f32_e32 v21, v21, v122
	v_cndmask_b32_e32 v10, v226, v10, vcc
	v_cmp_le_i32_e32 vcc, v73, v121
	v_add_u32_e32 v73, 11, v72
	v_sub_f32_e32 v10, v10, v122
	v_cndmask_b32_e32 v26, v226, v26, vcc
	v_cmp_le_i32_e32 vcc, v73, v1
	v_exp_f32_e32 v6, v6
	v_sub_f32_e32 v23, v23, v122
	v_cndmask_b32_e32 v11, v226, v11, vcc
	v_cmp_le_i32_e32 vcc, v73, v121
	v_add_u32_e32 v73, 16, v72
	v_sub_f32_e32 v11, v11, v122
	v_cndmask_b32_e32 v27, v226, v27, vcc
	v_cmp_le_i32_e32 vcc, v73, v1
	v_exp_f32_e32 v11, v11
	v_exp_f32_e32 v8, v8
	v_cndmask_b32_e32 v12, v226, v12, vcc
	v_cmp_le_i32_e32 vcc, v73, v121
	v_add_u32_e32 v73, 17, v72
	v_sub_f32_e32 v25, v25, v122
	v_cndmask_b32_e32 v28, v226, v28, vcc
	v_cmp_le_i32_e32 vcc, v73, v1
	v_exp_f32_e32 v10, v10
	v_sub_f32_e32 v27, v27, v122
	v_cndmask_b32_e32 v13, v226, v13, vcc
	v_cmp_le_i32_e32 vcc, v73, v121
	v_add_u32_e32 v73, 18, v72
	v_exp_f32_e32 v21, v21
	v_cndmask_b32_e32 v29, v226, v29, vcc
	v_cmp_le_i32_e32 vcc, v73, v1
	v_sub_f32_e32 v20, v20, v122
	v_exp_f32_e32 v23, v23
	v_cndmask_b32_e32 v14, v226, v14, vcc
	v_cmp_le_i32_e32 vcc, v73, v121
	v_add_u32_e32 v73, 19, v72
	v_sub_f32_e32 v22, v22, v122
	v_cndmask_b32_e32 v30, v226, v30, vcc
	v_cmp_le_i32_e32 vcc, v73, v1
	v_exp_f32_e32 v25, v25
	v_sub_f32_e32 v24, v24, v122
	v_cndmask_b32_e32 v15, v226, v15, vcc
	v_cmp_le_i32_e32 vcc, v73, v121
	v_add_u32_e32 v73, 24, v72
	v_exp_f32_e32 v27, v27
	v_cndmask_b32_e32 v31, v226, v31, vcc
	v_cmp_le_i32_e32 vcc, v73, v1
	v_sub_f32_e32 v26, v26, v122
	v_exp_f32_e32 v20, v20
	v_cndmask_b32_e32 v16, v226, v16, vcc
	v_cmp_le_i32_e32 vcc, v73, v121
	v_add_u32_e32 v73, 25, v72
	v_exp_f32_e32 v22, v22
	v_cndmask_b32_e32 v32, v226, v32, vcc
	v_cmp_le_i32_e32 vcc, v73, v1
	v_exp_f32_e32 v24, v24
	v_exp_f32_e32 v26, v26
	v_cndmask_b32_e32 v17, v226, v17, vcc
	v_cmp_le_i32_e32 vcc, v73, v121
	v_add_u32_e32 v73, 26, v72
	v_add_u32_e32 v72, 27, v72
	v_cndmask_b32_e32 v33, v226, v33, vcc
	v_cmp_le_i32_e32 vcc, v73, v1
	v_sub_f32_e32 v13, v13, v122
	v_sub_f32_e32 v15, v15, v122
	v_cndmask_b32_e32 v18, v226, v18, vcc
	v_cmp_le_i32_e32 vcc, v73, v121
	v_sub_f32_e32 v17, v17, v122
	v_mul_f32_e32 v5, v48, v5
	v_cndmask_b32_e32 v34, v226, v34, vcc
	v_cmp_le_i32_e32 vcc, v72, v1
	v_mul_f32_e32 v7, v48, v7
	v_mul_f32_e32 v9, v48, v9
	v_cndmask_b32_e32 v19, v226, v19, vcc
	v_cmp_le_i32_e32 vcc, v72, v121
	v_sub_f32_e32 v19, v19, v122
	v_mul_f32_e32 v11, v48, v11
	v_cndmask_b32_e32 v35, v226, v35, vcc
	v_sub_f32_e32 v12, v12, v122
	v_exp_f32_e32 v13, v13
	v_sub_f32_e32 v14, v14, v122
	v_exp_f32_e32 v15, v15
	v_sub_f32_e32 v16, v16, v122
	v_exp_f32_e32 v17, v17
	v_sub_f32_e32 v18, v18, v122
	v_exp_f32_e32 v19, v19
	v_exp_f32_e32 v12, v12
	v_sub_f32_e32 v29, v29, v122
	v_exp_f32_e32 v14, v14
	v_sub_f32_e32 v31, v31, v122
	v_exp_f32_e32 v16, v16
	v_sub_f32_e32 v33, v33, v122
	v_exp_f32_e32 v18, v18
	v_sub_f32_e32 v35, v35, v122
	v_fmac_f32_e32 v5, v48, v4
	v_fma_f32 v4, v48, v6, v7
	v_fmac_f32_e32 v9, v48, v8
	v_fma_f32 v6, v48, v10, v11
	v_mul_f32_e32 v21, v48, v21
	v_mul_f32_e32 v23, v48, v23
	v_mul_f32_e32 v25, v48, v25
	v_mul_f32_e32 v27, v48, v27
	v_exp_f32_e32 v29, v29
	v_sub_f32_e32 v28, v28, v122
	v_exp_f32_e32 v31, v31
	v_sub_f32_e32 v30, v30, v122
	v_exp_f32_e32 v33, v33
	v_sub_f32_e32 v32, v32, v122
	v_exp_f32_e32 v35, v35
	v_sub_f32_e32 v34, v34, v122
	v_add_f32_e32 v4, v5, v4
	v_add_f32_e32 v6, v9, v6
	v_add_u32_e32 v8, 0xc000, v56
	v_exp_f32_e32 v28, v28
	v_exp_f32_e32 v30, v30
	v_exp_f32_e32 v32, v32
	v_exp_f32_e32 v34, v34
	v_fmac_f32_e32 v21, v48, v20
	v_fma_f32 v5, v48, v22, v23
	ds_write2_b32 v8, v4, v6 offset1:2
	ds_write2_b32 v57, v7, v11 offset1:2
	v_fmac_f32_e32 v25, v48, v24
	v_fma_f32 v4, v48, v26, v27
	v_mul_f32_e32 v13, v48, v13
	v_mul_f32_e32 v15, v48, v15
	v_mul_f32_e32 v17, v48, v17
	v_mul_f32_e32 v19, v48, v19
	v_add_f32_e32 v5, v21, v5
	v_add_f32_e32 v4, v25, v4
	ds_write2_b32 v8, v5, v4 offset0:8 offset1:10
	ds_write2_b32 v57, v23, v27 offset0:8 offset1:10
	v_fmac_f32_e32 v13, v48, v12
	v_fma_f32 v4, v48, v14, v15
	v_fmac_f32_e32 v17, v48, v16
	v_fma_f32 v6, v48, v18, v19
	v_mul_f32_e32 v29, v48, v29
	v_mul_f32_e32 v31, v48, v31
	v_mul_f32_e32 v33, v48, v33
	v_mul_f32_e32 v35, v48, v35
	v_add_f32_e32 v4, v13, v4
	v_add_f32_e32 v6, v17, v6
	v_fmac_f32_e32 v29, v48, v28
	v_fma_f32 v5, v48, v30, v31
	ds_write2_b32 v8, v4, v6 offset0:4 offset1:6
	ds_write2_b32 v57, v15, v19 offset0:4 offset1:6
	v_fmac_f32_e32 v33, v48, v32
	v_fma_f32 v4, v48, v34, v35
	v_add_f32_e32 v5, v29, v5
	v_add_f32_e32 v4, v33, v4
	s_andn2_b64 vcc, exec, s[0:1]
	ds_write2_b32 v8, v5, v4 offset0:12 offset1:14
	ds_write2_b32 v57, v31, v35 offset0:12 offset1:14
	s_cbranch_vccnz .LBB0_827
	s_xor_b32 s0, s31, 0x4000
	v_add_u32_e32 v4, s0, v45
	s_waitcnt vmcnt(1)
	ds_write_b128 v4, v[36:39]
	s_waitcnt vmcnt(0)
	ds_write_b128 v4, v[40:43] offset:8192
